# v14
# speedup vs baseline: 1.0001x; 1.0001x over previous
_Z11prep_kernelPKfS0_S0_S0_PDF16_PfS1_:
	s_cmpk_gt_i32 s2, 0x1ff
	s_mov_b64 s[4:5], -1
	s_cbranch_scc0 .LBB0_4
	s_load_dwordx4 s[8:11], s[0:1], 0x10
	s_load_dwordx2 s[4:5], s[0:1], 0x30
	s_add_i32 s12, s2, 0xfffffe00
	s_cmpk_lt_u32 s12, 0x800
	v_lshl_or_b32 v1, s12, 8, v0
	s_waitcnt lgkmcnt(0)
	s_cselect_b32 s7, s9, s11
	s_cselect_b32 s6, s8, s10
	s_and_b32 s3, s12, 0xfffff800
	s_cmpk_eq_i32 s3, 0x800
	s_cselect_b32 s3, 0x80, 0
	s_bfe_u32 s8, s12, 0xa0001
	v_mov_b32_e32 v4, s8
	v_mov_b32_e32 v5, 0
	v_or_b32_e32 v2, 0xfff80000, v1
	v_mov_b32_e32 v3, -1
	s_mov_b64 s[8:9], 0
	s_mov_b64 s[10:11], 0x80000
	s_mov_b64 s[12:13], 0xbffff
	s_mov_b64 s[14:15], 0x1600
	s_mov_b64 s[16:17], 0x400
	s_mov_b64 s[18:19], 0xfffff
	v_mov_b64_e32 v[6:7], v[4:5]

_Z12gemm_persistILi0ELi4096ELi32ELi112EEvPKDF16_S1_PvPKfS4_S4_S4_PDF16_S5_iii:
	s_load_dwordx4 s[16:19], s[0:1], 0x48
	s_load_dword s3, s[0:1], 0x58
	s_waitcnt lgkmcnt(0)
	s_cmp_eq_u32 s17, 0
	s_cselect_b32 s18, 3, 11
	s_cselect_b32 s17, 0, 3
	v_readfirstlane_b32 s19, v0
	s_mul_i32 s4, s3, s17
	s_add_i32 s4, s4, s2
	s_cmpk_gt_i32 s4, 0xdff
	s_cbranch_scc1 .LBB1_30
	v_lshrrev_b32_e32 v1, 5, v0
	v_lshrrev_b32_e32 v4, 2, v0
	v_and_b32_e32 v1, 4, v1
	v_lshrrev_b32_e32 v2, 3, v0
	v_bfe_u32 v3, v0, 3, 2
	v_and_b32_e32 v4, 24, v4
	v_or3_b32 v3, v1, v3, v4
	v_or_b32_e32 v4, 64, v2
	s_movk_i32 s5, 0x60
	v_and_or_b32 v5, v4, s5, v3
	s_ashr_i32 s5, s4, 31
	s_lshr_b32 s5, s5, 29
	s_add_i32 s5, s4, s5
	s_lshr_b32 s30, s19, 6
	s_ashr_i32 s8, s5, 3
	s_and_b32 s5, s5, -8
	s_lshr_b32 s31, s19, 8
	s_lshl_b32 s10, s30, 10
	s_sub_i32 s4, s4, s5
	s_cmp_lt_i32 s4, 0
	s_movk_i32 s33, 0x1c1
	s_cselect_b32 s5, s33, 0x1c0
	s_mul_i32 s4, s5, s4
	s_add_i32 s4, s4, s8
	s_mul_hi_i32 s5, s4, 0x92492493
	s_add_i32 s5, s5, s4
	s_lshr_b32 s8, s5, 31
	s_ashr_i32 s5, s5, 9
	s_add_i32 s5, s5, s8
	s_lshl_b32 s8, s5, 3
	s_mulk_i32 s5, 0x380
	s_sub_i32 s4, s4, s5
	s_bfe_u32 s5, s4, 0x3001c
	s_add_i32 s5, s4, s5
	s_sext_i32_i16 s9, s5
	s_and_b32 s5, s5, 0xfff8
	s_sub_i32 s4, s4, s5
	s_load_dwordx4 s[20:23], s[0:1], 0x0
	s_load_dwordx2 s[6:7], s[0:1], 0x10
	s_sext_i32_i16 s4, s4
	s_lshr_b32 s28, s9, 3
	s_add_i32 s42, s8, s4
	s_ashr_i32 s43, s42, 31
	s_bfe_i64 s[4:5], s[28:29], 0x100000
	s_lshl_b64 s[8:9], s[42:43], 21
	s_lshl_b64 s[4:5], s[4:5], 21
	v_xor_b32_e32 v1, v2, v0
	s_waitcnt lgkmcnt(0)
	s_add_u32 s4, s22, s4
	v_lshlrev_b32_e32 v1, 4, v1
	s_addc_u32 s5, s23, s5
	s_add_i32 s43, s10, 0
	v_and_b32_e32 v1, 0x70, v1
	v_and_or_b32 v3, v2, 32, v3
	s_add_i32 s52, s43, 0x10000
	s_add_i32 s53, s43, 0x12000
	v_lshl_or_b32 v200, v3, 13, v1
	s_mov_b32 m0, s52
	s_add_u32 s44, s20, s8
	v_lshl_or_b32 v196, v5, 13, v1
	v_lshlrev_b32_e32 v2, 13, v2
	global_load_lds_dwordx4 v200, s[4:5]
	s_mov_b32 m0, s53
	s_addc_u32 s45, s21, s9
	s_add_i32 s54, s43, 0x2000
	v_or_b32_e32 v202, v2, v1
	global_load_lds_dwordx4 v196, s[4:5]
	s_mov_b32 m0, s43
	s_add_u32 s8, s4, 0x100000
	v_lshl_or_b32 v198, v4, 13, v1
	global_load_lds_dwordx4 v202, s[44:45]
	s_mov_b32 m0, s54
	s_addc_u32 s9, s5, 0
	s_add_i32 s55, s43, 0x14000
	global_load_lds_dwordx4 v198, s[44:45]
	s_mov_b32 m0, s55
	s_add_i32 s56, s43, 0x16000
	global_load_lds_dwordx4 v200, s[8:9]
	s_mov_b32 m0, s56
	v_mov_b32_e32 v205, 0
	global_load_lds_dwordx4 v196, s[8:9]
	s_add_u32 s8, s44, 0x100000
	s_addc_u32 s9, s45, 0
	s_add_i32 s57, s43, 0x4000
	v_mov_b32_e32 v201, v205
	s_mov_b32 m0, s57
	s_add_i32 s58, s43, 0x6000
	v_lshl_add_u64 v[4:5], s[4:5], 0, v[200:201]
	v_mov_b32_e32 v197, v205
	global_load_lds_dwordx4 v202, s[8:9]
	s_mov_b32 m0, s58
	s_add_i32 s59, s43, 0x18000
	s_mov_b64 s[24:25], 0x80
	v_lshl_add_u64 v[6:7], s[4:5], 0, v[196:197]
	v_mov_b32_e32 v203, v205
	global_load_lds_dwordx4 v198, s[8:9]
	v_lshl_add_u64 v[4:5], v[4:5], 0, s[24:25]
	s_mov_b32 m0, s59
	s_add_i32 s60, s43, 0x1a000
	v_lshl_add_u64 v[8:9], s[44:45], 0, v[202:203]
	v_mov_b32_e32 v199, v205
	global_load_lds_dwordx4 v[4:5], off
	v_lshl_add_u64 v[4:5], v[6:7], 0, s[24:25]
	s_mov_b32 m0, s60
	s_add_i32 s61, s43, 0x8000
	s_add_i32 s62, s43, 0xa000
	v_lshl_add_u64 v[10:11], s[44:45], 0, v[198:199]
	global_load_lds_dwordx4 v[4:5], off
	v_lshl_add_u64 v[4:5], v[8:9], 0, s[24:25]
	s_mov_b32 m0, s61
	s_add_u32 s8, s4, 0x100080
	global_load_lds_dwordx4 v[4:5], off
	v_lshl_add_u64 v[4:5], v[10:11], 0, s[24:25]
	s_mov_b32 m0, s62
	s_addc_u32 s9, s5, 0
	s_add_i32 s63, s43, 0x1c000
	global_load_lds_dwordx4 v[4:5], off
	s_mov_b32 m0, s63
	s_add_i32 s64, s43, 0x1e000
	global_load_lds_dwordx4 v200, s[8:9]
	s_mov_b32 m0, s64
	s_mov_b32 s29, 0
	global_load_lds_dwordx4 v196, s[8:9]
	s_load_dwordx2 s[26:27], s[0:1], 0x40
	s_load_dwordx8 s[8:15], s[0:1], 0x20
	s_waitcnt vmcnt(6)
	s_cmp_lg_u32 s31, 1
	s_barrier
	s_cbranch_scc1 .LBB1_3
	s_barrier
.LBB1_3:
	s_mov_b32 s98, s16
	s_mov_b32 s84, 0
	s_cmp_lg_u32 s16, 0
	s_cselect_b32 s83, 0x5e, 55
	s_cselect_b32 s97, 0x60, 56
	s_cselect_b32 s93, 0x5f, 56
	s_mul_i32 s96, s2, s93
	v_lshrrev_b32_e32 v3, 4, v0
	v_and_b32_e32 v4, 15, v0
	v_bfe_u32 v5, v0, 4, 2
	v_and_b32_e32 v7, 7, v0
	s_lshl_b32 s0, s30, 5
	s_sext_i32_i16 s76, s28
	v_lshl_or_b32 v207, s31, 6, v4
	v_bitop3_b32 v3, v3, v7, 3 bitop3:0x6c
	v_bitop3_b32 v7, v5, v7, 4 bitop3:0x36
	s_and_b32 s28, s0, 0x60
	v_lshlrev_b32_e32 v6, 7, v207
	v_lshlrev_b32_e32 v3, 4, v3
	v_lshlrev_b32_e32 v7, 4, v7
	v_or_b32_e32 v4, s28, v4
	s_cmp_lg_u32 s16, 0
	v_lshlrev_b32_e32 v206, 2, v0
	v_lshlrev_b32_e32 v232, 3, v206
	v_lshlrev_b32_e32 v233, 2, v206
	v_lshlrev_b32_e32 v0, 4, v0
	v_or_b32_e32 v8, v6, v3
	v_or_b32_e32 v6, v6, v7
	v_lshlrev_b32_e32 v4, 7, v4
	s_cselect_b64 s[0:1], -1, 0
	v_add_u32_e32 v208, v2, v1
	v_add_u32_e32 v0, 0, v0
	v_or_b32_e32 v222, v4, v3
	v_or_b32_e32 v223, v4, v7
	s_mul_i32 s65, s2, 0x70
	v_lshl_or_b32 v224, v5, 3, s28
	v_add_u32_e32 v210, 0x80000, v208
	v_mov_b32_e32 v211, v205
	v_mov_b32_e32 v209, v205
	s_and_b64 s[0:1], exec, s[0:1]
	s_movk_i32 s16, 0xe00
	v_add_u32_e32 v225, 0x20000, v0
	s_add_i32 s66, 0, 0x10000
	s_add_i32 s67, 0, 0x10800
	s_add_i32 s68, 0, 0x14000
	s_add_i32 s69, 0, 0x14800
	s_add_i32 s70, 0, 0x18000
	s_add_i32 s71, 0, 0x18800
	s_add_i32 s72, 0, 0x1c000
	s_add_i32 s73, 0, 0x1c800
	s_movk_i32 s74, 0x7000
	v_add_u32_e32 v226, 0, v8
	v_add_u32_e32 v227, 0, v6
	s_mov_b32 s30, s29
	s_mov_b32 s34, s29
	s_mov_b32 s28, 0
	s_branch .LBB1_5

.LBB1_9:
	s_add_i32 s82, s48, 2
	s_cmp_lt_u32 s84, s97
	s_cselect_b32 s85, 1, 0
	s_cmp_lg_u32 s84, 0
	s_cselect_b32 s93, 1, 0
	s_and_b32 s93, s93, s85
	s_add_u32 s85, s85, s93
	s_min_u32 s92, s84, s83
	s_add_i32 s93, s96, s92
	s_waitcnt lgkmcnt(0)
	s_cmp_lg_u32 s98, 0
	s_cbranch_scc0 .Lsj_kind0
	s_sub_u32 s94, s93, 0x5800
	s_cmp_ge_u32 s93, 0x5800
	s_cselect_b32 s93, s94, s93
	s_cmp_ge_u32 s93, 0x2c00
	s_cselect_b32 s94, 1, 0
	s_cselect_b32 s99, s10, s8
	s_cselect_b32 s100, s11, s9
	s_mul_i32 s95, s94, 0x2c00
	s_sub_u32 s93, s93, s95
	s_cmp_ge_u32 s93, 0x1600
	s_cselect_b32 s95, 0x600, 0
	s_add_u32 s95, s95, 0x600
	s_add_u32 s93, s93, s95
	s_lshl_b32 s95, s93, 14
	s_add_u32 s90, s99, s95
	s_addc_u32 s91, s100, 0
	s_lshr_b32 s95, s93, 7
	s_lshl_b32 s95, s95, 8
	s_and_b32 s93, s93, 0x7f
	s_add_u32 s95, s95, s93
	s_lshl_b32 s94, s94, 7
	s_add_u32 s95, s95, s94
	s_lshl_b32 s95, s95, 13
	s_add_u32 s88, s14, s95
	s_addc_u32 s89, s15, 0
	s_branch .Lsj_evdone
.Lsj_kind0:
	s_lshl_b32 s95, s93, 14
	s_add_u32 s90, s12, s95
	s_addc_u32 s91, s13, 0
	s_lshl_b32 s95, s93, 13
	s_add_u32 s88, s26, s95
	s_addc_u32 s89, s27, 0
.Lsj_evdone:
	v_add_u32_e32 v132, s66, v222
	v_add_u32_e32 v133, s66, v223
	ds_read_b128 v[148:151], v132
	ds_read_b128 v[152:155], v133
	v_add_u32_e32 v132, s67, v222
	v_add_u32_e32 v133, s67, v223
	ds_read_b128 v[156:159], v132
	ds_read_b128 v[160:163], v133
	v_add_u32_e32 v132, s68, v222
	v_add_u32_e32 v136, s68, v223
	v_add_u32_e32 v140, s69, v222
	v_add_u32_e32 v144, s69, v223
	v_lshl_add_u64 v[194:195], s[44:45], 0, v[208:209]
	s_add_i32 m0, s43, 0xc000
	ds_read_b128 v[132:135], v132
	ds_read_b128 v[136:139], v136
	ds_read_b128 v[140:143], v140
	ds_read_b128 v[144:147], v144
	ds_read_b128 v[166:169], v226
	ds_read_b128 v[170:173], v226 offset:2048
	ds_read_b128 v[174:177], v227
	ds_read_b128 v[178:181], v227 offset:2048
	ds_read_b128 v[182:185], v226 offset:4096
	ds_read_b128 v[186:189], v226 offset:6144
	ds_read_b128 v[190:193], v227 offset:4096
	ds_read_b128 v[214:217], v227 offset:6144
	global_load_lds_dwordx4 v[194:195], off
	v_lshl_add_u64 v[194:195], s[44:45], 0, v[210:211]
	s_add_i32 m0, s43, 0xe000
	s_nop 0
	global_load_lds_dwordx4 v[194:195], off
	s_waitcnt vmcnt(8)
	s_waitcnt lgkmcnt(0)
	s_barrier
	s_setprio 1
	s_waitcnt lgkmcnt(0)
	v_mfma_f32_16x16x32_f16 v[128:131], v[148:151], v[166:169], v[128:131]
	v_mfma_f32_16x16x32_f16 v[128:131], v[152:155], v[174:177], v[128:131]
	v_mfma_f32_16x16x32_f16 v[120:123], v[160:163], v[174:177], v[120:123]
	v_mfma_f32_16x16x32_f16 v[120:123], v[156:159], v[166:169], v[120:123]
	v_mfma_f32_16x16x32_f16 v[104:107], v[156:159], v[170:173], v[104:107]
	v_mfma_f32_16x16x32_f16 v[104:107], v[160:163], v[178:181], v[104:107]
	v_mfma_f32_16x16x32_f16 v[112:115], v[152:155], v[178:181], v[112:115]
	v_mfma_f32_16x16x32_f16 v[112:115], v[148:151], v[170:173], v[112:115]
	v_mfma_f32_16x16x32_f16 v[96:99], v[148:151], v[182:185], v[96:99]
	v_mfma_f32_16x16x32_f16 v[96:99], v[152:155], v[190:193], v[96:99]
	v_mfma_f32_16x16x32_f16 v[88:91], v[160:163], v[190:193], v[88:91]
	v_mfma_f32_16x16x32_f16 v[88:91], v[156:159], v[182:185], v[88:91]
	v_mfma_f32_16x16x32_f16 v[72:75], v[156:159], v[186:189], v[72:75]
	v_mfma_f32_16x16x32_f16 v[72:75], v[160:163], v[214:217], v[72:75]
	v_mfma_f32_16x16x32_f16 v[80:83], v[152:155], v[214:217], v[80:83]
	v_mfma_f32_16x16x32_f16 v[80:83], v[148:151], v[186:189], v[80:83]
	s_setprio 0
	s_setprio 1
	v_mfma_f32_16x16x32_f16 v[124:127], v[132:135], v[166:169], v[124:127]
	v_mfma_f32_16x16x32_f16 v[124:127], v[136:139], v[174:177], v[124:127]
	v_mfma_f32_16x16x32_f16 v[116:119], v[144:147], v[174:177], v[116:119]
	v_mfma_f32_16x16x32_f16 v[116:119], v[140:143], v[166:169], v[116:119]
	v_mfma_f32_16x16x32_f16 v[100:103], v[140:143], v[170:173], v[100:103]
	v_mfma_f32_16x16x32_f16 v[100:103], v[144:147], v[178:181], v[100:103]
	v_mfma_f32_16x16x32_f16 v[108:111], v[136:139], v[178:181], v[108:111]
	v_mfma_f32_16x16x32_f16 v[108:111], v[132:135], v[170:173], v[108:111]
	v_mfma_f32_16x16x32_f16 v[92:95], v[132:135], v[182:185], v[92:95]
	v_mfma_f32_16x16x32_f16 v[92:95], v[136:139], v[190:193], v[92:95]
	v_mfma_f32_16x16x32_f16 v[84:87], v[144:147], v[190:193], v[84:87]
	v_mfma_f32_16x16x32_f16 v[84:87], v[140:143], v[182:185], v[84:87]
	v_mfma_f32_16x16x32_f16 v[68:71], v[140:143], v[186:189], v[68:71]
	v_mfma_f32_16x16x32_f16 v[68:71], v[144:147], v[214:217], v[68:71]
	v_mfma_f32_16x16x32_f16 v[76:79], v[136:139], v[214:217], v[76:79]
	v_mfma_f32_16x16x32_f16 v[76:79], v[132:135], v[186:189], v[76:79]
	s_setprio 0
	s_barrier
	s_add_u32 s28, s44, 0xfff00080
	s_addc_u32 s46, s45, -1
	s_cmp_eq_u32 s48, 60
	s_cselect_b32 s49, s31, s46
	s_cselect_b32 s47, s35, s81
	s_cselect_b32 s46, s78, s80
	s_mov_b32 m0, s52
	s_cselect_b32 s48, s77, s28
	v_lshl_add_u64 v[214:215], s[46:47], 0, v[200:201]
	s_add_u32 s50, s46, 0x100000
	ds_read_b128 v[188:191], v226 offset:16384
	ds_read_b128 v[176:179], v226 offset:18432
	ds_read_b128 v[192:195], v227 offset:16384
	ds_read_b128 v[180:183], v227 offset:18432
	ds_read_b128 v[172:175], v226 offset:20480
	ds_read_b128 v[164:167], v226 offset:22528
	ds_read_b128 v[184:187], v227 offset:20480
	ds_read_b128 v[168:171], v227 offset:22528
	global_load_lds_dwordx4 v[214:215], off
	v_lshl_add_u64 v[216:217], s[46:47], 0, v[196:197]
	s_mov_b32 m0, s53
	s_addc_u32 s51, s47, 0
	global_load_lds_dwordx4 v[216:217], off
	v_lshl_add_u64 v[218:219], s[50:51], 0, v[200:201]
	s_mov_b32 m0, s55
	v_lshl_add_u64 v[220:221], s[48:49], 0, v[198:199]
	global_load_lds_dwordx4 v[218:219], off
	v_lshl_add_u64 v[218:219], s[50:51], 0, v[196:197]
	s_mov_b32 m0, s56
	s_nop 0
	global_load_lds_dwordx4 v[218:219], off
	v_lshl_add_u64 v[218:219], s[48:49], 0, v[202:203]
	s_mov_b32 m0, s43
	s_nop 0
	global_load_lds_dwordx4 v[218:219], off
	s_mov_b32 m0, s54
	s_nop 0
	global_load_lds_dwordx4 v[220:221], off
	s_sub_u32 s93, s84, 1
	s_cmp_le_u32 s93, s83
	s_cbranch_scc0 .Lsj_nost
	v_cvt_pkrtz_f16_f32 v0, v0, v1
	v_cvt_pkrtz_f16_f32 v1, v2, v3
	v_cvt_pkrtz_f16_f32 v2, v228, v229
	v_cvt_pkrtz_f16_f32 v3, v230, v231
	v_add_u32_e32 v0, 0x20002, v0
	v_add_u32_e32 v1, 0x20002, v1
	v_add_u32_e32 v2, 0x20002, v2
	v_add_u32_e32 v3, 0x20002, v3
	v_and_b32_e32 v0, 0xfffcfffc, v0
	v_and_b32_e32 v1, 0xfffcfffc, v1
	v_and_b32_e32 v2, 0xfffcfffc, v2
	v_and_b32_e32 v3, 0xfffcfffc, v3
	global_store_dwordx4 v233, v[0:3], s[86:87]
.Lsj_nost:
	s_cmp_lg_u32 s85, 0
	s_cbranch_scc0 .Lsj_p2n
	global_load_dwordx4 v[0:3], v232, s[90:91] nt
	global_load_dwordx4 v[228:231], v232, s[90:91] offset:16 nt
	s_mov_b64 s[86:87], s[88:89]
	s_cmp_eq_u32 s85, 2
	s_cbranch_scc0 .Lsj_p2m
	s_waitcnt vmcnt(11)
	s_branch .Lsj_p2e
.Lsj_p2m:
	s_waitcnt vmcnt(10)
	s_branch .Lsj_p2e
.Lsj_p2n:
	s_waitcnt vmcnt(8)
.Lsj_p2e:
	s_waitcnt lgkmcnt(0)
	s_barrier
	s_setprio 1
	s_waitcnt lgkmcnt(0)
	v_mfma_f32_16x16x32_f16 v[64:67], v[148:151], v[188:191], v[64:67]
	v_mfma_f32_16x16x32_f16 v[64:67], v[152:155], v[192:195], v[64:67]
	v_mfma_f32_16x16x32_f16 v[56:59], v[160:163], v[192:195], v[56:59]
	v_mfma_f32_16x16x32_f16 v[56:59], v[156:159], v[188:191], v[56:59]
	v_mfma_f32_16x16x32_f16 v[40:43], v[156:159], v[176:179], v[40:43]
	v_mfma_f32_16x16x32_f16 v[40:43], v[160:163], v[180:183], v[40:43]
	v_mfma_f32_16x16x32_f16 v[48:51], v[152:155], v[180:183], v[48:51]
	v_mfma_f32_16x16x32_f16 v[48:51], v[148:151], v[176:179], v[48:51]
	v_mfma_f32_16x16x32_f16 v[32:35], v[148:151], v[172:175], v[32:35]
	v_mfma_f32_16x16x32_f16 v[32:35], v[152:155], v[184:187], v[32:35]
	v_mfma_f32_16x16x32_f16 v[24:27], v[160:163], v[184:187], v[24:27]
	v_mfma_f32_16x16x32_f16 v[24:27], v[156:159], v[172:175], v[24:27]
	v_mfma_f32_16x16x32_f16 v[8:11], v[156:159], v[164:167], v[8:11]
	v_mfma_f32_16x16x32_f16 v[8:11], v[160:163], v[168:171], v[8:11]
	v_mfma_f32_16x16x32_f16 v[16:19], v[152:155], v[168:171], v[16:19]
	v_mfma_f32_16x16x32_f16 v[16:19], v[148:151], v[164:167], v[16:19]
	s_setprio 0
	s_setprio 1
	v_mfma_f32_16x16x32_f16 v[60:63], v[132:135], v[188:191], v[60:63]
	v_mfma_f32_16x16x32_f16 v[60:63], v[136:139], v[192:195], v[60:63]
	v_mfma_f32_16x16x32_f16 v[52:55], v[144:147], v[192:195], v[52:55]
	v_mfma_f32_16x16x32_f16 v[52:55], v[140:143], v[188:191], v[52:55]
	v_mfma_f32_16x16x32_f16 v[36:39], v[140:143], v[176:179], v[36:39]
	v_mfma_f32_16x16x32_f16 v[36:39], v[144:147], v[180:183], v[36:39]
	v_mfma_f32_16x16x32_f16 v[44:47], v[136:139], v[180:183], v[44:47]
	v_mfma_f32_16x16x32_f16 v[44:47], v[132:135], v[176:179], v[44:47]
	v_mfma_f32_16x16x32_f16 v[28:31], v[132:135], v[172:175], v[28:31]
	v_mfma_f32_16x16x32_f16 v[28:31], v[136:139], v[184:187], v[28:31]
	v_mfma_f32_16x16x32_f16 v[20:23], v[144:147], v[184:187], v[20:23]
	v_mfma_f32_16x16x32_f16 v[20:23], v[140:143], v[172:175], v[20:23]
	v_mfma_f32_16x16x32_f16 v[4:7], v[140:143], v[164:167], v[4:7]
	v_mfma_f32_16x16x32_f16 v[4:7], v[144:147], v[168:171], v[4:7]
	v_mfma_f32_16x16x32_f16 v[12:15], v[136:139], v[168:171], v[12:15]
	v_mfma_f32_16x16x32_f16 v[12:15], v[132:135], v[164:167], v[12:15]
	s_setprio 0
	s_barrier
	v_add_u32_e32 v132, s70, v222
	s_add_u32 s48, s48, 0x100000
	v_add_u32_e32 v133, s70, v223
	ds_read_b128 v[148:151], v132
	ds_read_b128 v[152:155], v133
	v_add_u32_e32 v132, s71, v222
	s_addc_u32 s49, s49, 0
	s_mov_b32 m0, s57
	v_add_u32_e32 v133, s71, v223
	ds_read_b128 v[156:159], v132
	ds_read_b128 v[160:163], v133
	v_add_u32_e32 v132, s72, v222
	v_add_u32_e32 v136, s72, v223
	v_add_u32_e32 v140, s73, v222
	v_add_u32_e32 v144, s73, v223
	v_lshl_add_u64 v[212:213], s[48:49], 0, v[202:203]
	ds_read_b128 v[132:135], v132
	ds_read_b128 v[136:139], v136
	ds_read_b128 v[140:143], v140
	ds_read_b128 v[144:147], v144
	ds_read_b128 v[188:191], v226 offset:32768
	ds_read_b128 v[176:179], v226 offset:34816
	ds_read_b128 v[192:195], v227 offset:32768
	ds_read_b128 v[180:183], v227 offset:34816
	ds_read_b128 v[172:175], v226 offset:36864
	ds_read_b128 v[164:167], v226 offset:38912
	ds_read_b128 v[184:187], v227 offset:36864
	ds_read_b128 v[168:171], v227 offset:38912
	global_load_lds_dwordx4 v[212:213], off
	v_lshl_add_u64 v[212:213], s[48:49], 0, v[198:199]
	s_mov_b32 m0, s58
	s_nop 0
	global_load_lds_dwordx4 v[212:213], off
	s_cmp_lg_u32 s85, 0
	s_cbranch_scc0 .Lsj_p3n
	s_cmp_eq_u32 s85, 2
	s_cbranch_scc0 .Lsj_p3m
	s_waitcnt vmcnt(11)
	s_branch .Lsj_p3e

.Lsj_p3e:
	s_waitcnt lgkmcnt(0)
	s_barrier
	s_setprio 1
	s_waitcnt lgkmcnt(0)
	v_mfma_f32_16x16x32_f16 v[128:131], v[148:151], v[188:191], v[128:131]
	v_mfma_f32_16x16x32_f16 v[128:131], v[152:155], v[192:195], v[128:131]
	v_mfma_f32_16x16x32_f16 v[120:123], v[160:163], v[192:195], v[120:123]
	v_mfma_f32_16x16x32_f16 v[120:123], v[156:159], v[188:191], v[120:123]
	v_mfma_f32_16x16x32_f16 v[104:107], v[156:159], v[176:179], v[104:107]
	v_mfma_f32_16x16x32_f16 v[104:107], v[160:163], v[180:183], v[104:107]
	v_mfma_f32_16x16x32_f16 v[112:115], v[152:155], v[180:183], v[112:115]
	v_mfma_f32_16x16x32_f16 v[112:115], v[148:151], v[176:179], v[112:115]
	v_mfma_f32_16x16x32_f16 v[96:99], v[148:151], v[172:175], v[96:99]
	v_mfma_f32_16x16x32_f16 v[96:99], v[152:155], v[184:187], v[96:99]
	v_mfma_f32_16x16x32_f16 v[88:91], v[160:163], v[184:187], v[88:91]
	v_mfma_f32_16x16x32_f16 v[88:91], v[156:159], v[172:175], v[88:91]
	v_mfma_f32_16x16x32_f16 v[72:75], v[156:159], v[164:167], v[72:75]
	v_mfma_f32_16x16x32_f16 v[72:75], v[160:163], v[168:171], v[72:75]
	v_mfma_f32_16x16x32_f16 v[80:83], v[152:155], v[168:171], v[80:83]
	v_mfma_f32_16x16x32_f16 v[80:83], v[148:151], v[164:167], v[80:83]
	s_setprio 0
	s_setprio 1
	v_mfma_f32_16x16x32_f16 v[124:127], v[132:135], v[188:191], v[124:127]
	v_mfma_f32_16x16x32_f16 v[124:127], v[136:139], v[192:195], v[124:127]
	v_mfma_f32_16x16x32_f16 v[116:119], v[144:147], v[192:195], v[116:119]
	v_mfma_f32_16x16x32_f16 v[116:119], v[140:143], v[188:191], v[116:119]
	v_mfma_f32_16x16x32_f16 v[100:103], v[140:143], v[176:179], v[100:103]
	v_mfma_f32_16x16x32_f16 v[100:103], v[144:147], v[180:183], v[100:103]
	v_mfma_f32_16x16x32_f16 v[108:111], v[136:139], v[180:183], v[108:111]
	v_mfma_f32_16x16x32_f16 v[108:111], v[132:135], v[176:179], v[108:111]
	v_mfma_f32_16x16x32_f16 v[92:95], v[132:135], v[172:175], v[92:95]
	v_mfma_f32_16x16x32_f16 v[92:95], v[136:139], v[184:187], v[92:95]
	v_mfma_f32_16x16x32_f16 v[84:87], v[144:147], v[184:187], v[84:87]
	v_mfma_f32_16x16x32_f16 v[84:87], v[140:143], v[172:175], v[84:87]
	v_mfma_f32_16x16x32_f16 v[68:71], v[140:143], v[164:167], v[68:71]
	v_mfma_f32_16x16x32_f16 v[68:71], v[144:147], v[168:171], v[68:71]
	v_mfma_f32_16x16x32_f16 v[76:79], v[136:139], v[168:171], v[76:79]
	v_mfma_f32_16x16x32_f16 v[76:79], v[132:135], v[164:167], v[76:79]
	s_setprio 0
	s_barrier
	s_mov_b32 m0, s59
	v_lshl_add_u64 v[212:213], v[214:215], 0, s[24:25]
	s_add_u32 s4, s46, 0x100080
	ds_read_b128 v[164:167], v226 offset:49152
	ds_read_b128 v[168:171], v226 offset:51200
	ds_read_b128 v[172:175], v227 offset:49152
	ds_read_b128 v[176:179], v227 offset:51200
	ds_read_b128 v[180:183], v226 offset:53248
	ds_read_b128 v[184:187], v226 offset:55296
	ds_read_b128 v[188:191], v227 offset:53248
	ds_read_b128 v[192:195], v227 offset:55296
	global_load_lds_dwordx4 v[212:213], off
	v_lshl_add_u64 v[212:213], v[216:217], 0, s[24:25]
	s_mov_b32 m0, s60
	s_addc_u32 s5, s47, 0
	global_load_lds_dwordx4 v[212:213], off
	v_lshl_add_u64 v[212:213], s[4:5], 0, v[200:201]
	s_mov_b32 m0, s63
	s_nop 0
	global_load_lds_dwordx4 v[212:213], off
	v_lshl_add_u64 v[212:213], s[4:5], 0, v[196:197]
	s_mov_b32 m0, s64
	s_nop 0
	global_load_lds_dwordx4 v[212:213], off
	v_lshl_add_u64 v[212:213], v[218:219], 0, s[24:25]
	s_mov_b32 m0, s61
	s_nop 0
	global_load_lds_dwordx4 v[212:213], off
	v_lshl_add_u64 v[212:213], v[220:221], 0, s[24:25]
	s_mov_b32 m0, s62
	s_nop 0
	global_load_lds_dwordx4 v[212:213], off
	s_cmp_lg_u32 s85, 0
	s_cbranch_scc0 .Lsj_p4n
	s_cmp_eq_u32 s85, 2
	s_cbranch_scc0 .Lsj_p4m
	s_waitcnt vmcnt(11)
	s_branch .Lsj_p4e

.Lsj_p4e:
	s_waitcnt lgkmcnt(0)
	s_barrier
	s_setprio 1
	s_waitcnt lgkmcnt(0)
	v_mfma_f32_16x16x32_f16 v[64:67], v[148:151], v[164:167], v[64:67]
	v_mfma_f32_16x16x32_f16 v[64:67], v[152:155], v[172:175], v[64:67]
	v_mfma_f32_16x16x32_f16 v[56:59], v[160:163], v[172:175], v[56:59]
	v_mfma_f32_16x16x32_f16 v[56:59], v[156:159], v[164:167], v[56:59]
	v_mfma_f32_16x16x32_f16 v[40:43], v[156:159], v[168:171], v[40:43]
	v_mfma_f32_16x16x32_f16 v[40:43], v[160:163], v[176:179], v[40:43]
	v_mfma_f32_16x16x32_f16 v[48:51], v[152:155], v[176:179], v[48:51]
	v_mfma_f32_16x16x32_f16 v[48:51], v[148:151], v[168:171], v[48:51]
	v_mfma_f32_16x16x32_f16 v[32:35], v[148:151], v[180:183], v[32:35]
	v_mfma_f32_16x16x32_f16 v[32:35], v[152:155], v[188:191], v[32:35]
	v_mfma_f32_16x16x32_f16 v[24:27], v[160:163], v[188:191], v[24:27]
	v_mfma_f32_16x16x32_f16 v[24:27], v[156:159], v[180:183], v[24:27]
	v_mfma_f32_16x16x32_f16 v[8:11], v[156:159], v[184:187], v[8:11]
	v_mfma_f32_16x16x32_f16 v[8:11], v[160:163], v[192:195], v[8:11]
	v_mfma_f32_16x16x32_f16 v[16:19], v[152:155], v[192:195], v[16:19]
	v_mfma_f32_16x16x32_f16 v[16:19], v[148:151], v[184:187], v[16:19]
	s_setprio 0
	s_setprio 1
	v_mfma_f32_16x16x32_f16 v[60:63], v[132:135], v[164:167], v[60:63]
	v_mfma_f32_16x16x32_f16 v[60:63], v[136:139], v[172:175], v[60:63]
	v_mfma_f32_16x16x32_f16 v[52:55], v[144:147], v[172:175], v[52:55]
	v_mfma_f32_16x16x32_f16 v[52:55], v[140:143], v[164:167], v[52:55]
	v_mfma_f32_16x16x32_f16 v[36:39], v[140:143], v[168:171], v[36:39]
	v_mfma_f32_16x16x32_f16 v[36:39], v[144:147], v[176:179], v[36:39]
	v_mfma_f32_16x16x32_f16 v[44:47], v[136:139], v[176:179], v[44:47]
	v_mfma_f32_16x16x32_f16 v[44:47], v[132:135], v[168:171], v[44:47]
	v_mfma_f32_16x16x32_f16 v[28:31], v[132:135], v[180:183], v[28:31]
	v_mfma_f32_16x16x32_f16 v[28:31], v[136:139], v[188:191], v[28:31]
	v_mfma_f32_16x16x32_f16 v[20:23], v[144:147], v[188:191], v[20:23]
	v_mfma_f32_16x16x32_f16 v[20:23], v[140:143], v[180:183], v[20:23]
	v_mfma_f32_16x16x32_f16 v[4:7], v[140:143], v[184:187], v[4:7]
	v_mfma_f32_16x16x32_f16 v[4:7], v[144:147], v[192:195], v[4:7]
	v_mfma_f32_16x16x32_f16 v[12:15], v[136:139], v[192:195], v[12:15]
	v_mfma_f32_16x16x32_f16 v[12:15], v[132:135], v[184:187], v[12:15]
	s_setprio 0
	s_barrier
	s_add_i32 s84, s84, 1
	s_add_u32 s80, s80, 0x100
	s_addc_u32 s81, s81, 0
	s_add_u32 s44, s44, 0x100
	s_addc_u32 s45, s45, 0
	s_cmp_gt_u32 s82, 61
	s_cbranch_scc1 .LBB1_4
	s_mov_b32 s48, s82
	s_branch .LBB1_9

.LBB1_30:
	s_endpgm
	s_nop 0
	s_nop 0
	s_nop 0
	s_nop 0
	s_nop 0
	s_nop 0
	s_nop 0
	s_nop 0
	s_nop 0
	s_nop 0
	s_nop 0
	s_nop 0
	s_nop 0
	s_nop 0
	s_nop 0
	s_nop 0
	s_nop 0
	s_nop 0
	s_nop 0
	s_nop 0
	s_nop 0
	s_nop 0
	s_nop 0
	s_nop 0
	s_nop 0
	s_nop 0
	s_nop 0
	s_nop 0
	s_nop 0
	s_nop 0
	s_nop 0
	s_nop 0
	s_nop 0
	s_nop 0
	s_nop 0
	s_nop 0
	s_nop 0
	s_nop 0
	s_nop 0
	s_nop 0
	s_nop 0
	s_nop 0
	s_nop 0
	s_nop 0
	s_nop 0
	s_nop 0
	s_nop 0
	s_nop 0
	s_nop 0
	s_nop 0
	s_nop 0
	s_endpgm

	.amdhsa_kernel _Z12gemm_persistILi0ELi4096ELi32ELi112EEvPKDF16_S1_PvPKfS4_S4_S4_PDF16_S5_iii
		.amdhsa_group_segment_fixed_size 0
		.amdhsa_private_segment_fixed_size 0
		.amdhsa_kernarg_size 344
		.amdhsa_user_sgpr_count 2
		.amdhsa_user_sgpr_dispatch_ptr 0
		.amdhsa_user_sgpr_queue_ptr 0
		.amdhsa_user_sgpr_kernarg_segment_ptr 1
		.amdhsa_user_sgpr_dispatch_id 0
		.amdhsa_user_sgpr_kernarg_preload_length 0
		.amdhsa_user_sgpr_kernarg_preload_offset 0
		.amdhsa_user_sgpr_private_segment_size 0
		.amdhsa_uses_dynamic_stack 0
		.amdhsa_enable_private_segment 0
		.amdhsa_system_sgpr_workgroup_id_x 1
		.amdhsa_system_sgpr_workgroup_id_y 0
		.amdhsa_system_sgpr_workgroup_id_z 0
		.amdhsa_system_sgpr_workgroup_info 0
		.amdhsa_system_vgpr_workitem_id 0
		.amdhsa_next_free_vgpr 236
		.amdhsa_next_free_sgpr 101
		.amdhsa_accum_offset 236
		.amdhsa_reserve_vcc 1
		.amdhsa_float_round_mode_32 0
		.amdhsa_float_round_mode_16_64 0
		.amdhsa_float_denorm_mode_32 3
		.amdhsa_float_denorm_mode_16_64 3
		.amdhsa_dx10_clamp 1
		.amdhsa_ieee_mode 1
		.amdhsa_fp16_overflow 0
		.amdhsa_tg_split 0
		.amdhsa_exception_fp_ieee_invalid_op 0
		.amdhsa_exception_fp_denorm_src 0
		.amdhsa_exception_fp_ieee_div_zero 0
		.amdhsa_exception_fp_ieee_overflow 0
		.amdhsa_exception_fp_ieee_underflow 0
		.amdhsa_exception_fp_ieee_inexact 0
		.amdhsa_exception_int_div_zero 0
	.end_amdhsa_kernel

amdhsa.kernels:
  - .agpr_count:     4
    .args:
      - .actual_access:  read_only
        .address_space:  global
        .offset:         0
        .size:           8
        .value_kind:     global_buffer
      - .actual_access:  read_only
        .address_space:  global
        .offset:         8
        .size:           8
        .value_kind:     global_buffer
      - .actual_access:  read_only
        .address_space:  global
        .offset:         16
        .size:           8
        .value_kind:     global_buffer
      - .actual_access:  read_only
        .address_space:  global
        .offset:         24
        .size:           8
        .value_kind:     global_buffer
      - .actual_access:  write_only
        .address_space:  global
        .offset:         32
        .size:           8
        .value_kind:     global_buffer
      - .actual_access:  write_only
        .address_space:  global
        .offset:         40
        .size:           8
        .value_kind:     global_buffer
      - .actual_access:  write_only
        .address_space:  global
        .offset:         48
        .size:           8
        .value_kind:     global_buffer
    .group_segment_fixed_size: 4352
    .kernarg_segment_align: 8
    .kernarg_segment_size: 56
    .language:       OpenCL C
    .language_version:
      - 2
      - 0
    .max_flat_workgroup_size: 256
    .name:           _Z11prep_kernelPKfS0_S0_S0_PDF16_PfS1_
    .private_segment_fixed_size: 0
    .sgpr_count:     26
    .sgpr_spill_count: 0
    .symbol:         _Z11prep_kernelPKfS0_S0_S0_PDF16_PfS1_.kd
    .uniform_work_group_size: 1
    .uses_dynamic_stack: false
    .vgpr_count:     56
    .vgpr_spill_count: 0
    .wavefront_size: 64
  - .agpr_count:     0
    .args:
      - .address_space:  global
        .offset:         0
        .size:           8
        .value_kind:     global_buffer
      - .address_space:  global
        .offset:         8
        .size:           8
        .value_kind:     global_buffer
      - .actual_access:  write_only
        .address_space:  global
        .offset:         16
        .size:           8
        .value_kind:     global_buffer
      - .actual_access:  read_only
        .address_space:  global
        .offset:         24
        .size:           8
        .value_kind:     global_buffer
      - .address_space:  global
        .offset:         32
        .size:           8
        .value_kind:     global_buffer
      - .address_space:  global
        .offset:         40
        .size:           8
        .value_kind:     global_buffer
      - .address_space:  global
        .offset:         48
        .size:           8
        .value_kind:     global_buffer
      - .actual_access:  write_only
        .address_space:  global
        .offset:         56
        .size:           8
        .value_kind:     global_buffer
      - .actual_access:  write_only
        .address_space:  global
        .offset:         64
        .size:           8
        .value_kind:     global_buffer
      - .offset:         72
        .size:           4
        .value_kind:     by_value
      - .offset:         76
        .size:           4
        .value_kind:     by_value
      - .offset:         80
        .size:           4
        .value_kind:     by_value
      - .offset:         88
        .size:           4
        .value_kind:     hidden_block_count_x
      - .offset:         92
        .size:           4
        .value_kind:     hidden_block_count_y
      - .offset:         96
        .size:           4
        .value_kind:     hidden_block_count_z
      - .offset:         100
        .size:           2
        .value_kind:     hidden_group_size_x
      - .offset:         102
        .size:           2
        .value_kind:     hidden_group_size_y
      - .offset:         104
        .size:           2
        .value_kind:     hidden_group_size_z
      - .offset:         106
        .size:           2
        .value_kind:     hidden_remainder_x
      - .offset:         108
        .size:           2
        .value_kind:     hidden_remainder_y
      - .offset:         110
        .size:           2
        .value_kind:     hidden_remainder_z
      - .offset:         128
        .size:           8
        .value_kind:     hidden_global_offset_x
      - .offset:         136
        .size:           8
        .value_kind:     hidden_global_offset_y
      - .offset:         144
        .size:           8
        .value_kind:     hidden_global_offset_z
      - .offset:         152
        .size:           2
        .value_kind:     hidden_grid_dims
      - .offset:         208
        .size:           4
        .value_kind:     hidden_dynamic_lds_size
    .group_segment_fixed_size: 0
    .kernarg_segment_align: 8
    .kernarg_segment_size: 344
    .language:       OpenCL C
    .language_version:
      - 2
      - 0
    .max_flat_workgroup_size: 512
    .name:           _Z12gemm_persistILi0ELi4096ELi32ELi112EEvPKDF16_S1_PvPKfS4_S4_S4_PDF16_S5_iii
    .private_segment_fixed_size: 0
    .sgpr_count:     107
    .sgpr_spill_count: 0
    .symbol:         _Z12gemm_persistILi0ELi4096ELi32ELi112EEvPKDF16_S1_PvPKfS4_S4_S4_PDF16_S5_iii.kd
    .uniform_work_group_size: 1
    .uses_dynamic_stack: false
    .vgpr_count:     236
    .vgpr_spill_count: 0
    .wavefront_size: 64
  - .agpr_count:     0
    .args:
      - .address_space:  global
        .offset:         0
        .size:           8
        .value_kind:     global_buffer
      - .address_space:  global
        .offset:         8
        .size:           8
        .value_kind:     global_buffer
      - .actual_access:  write_only
        .address_space:  global
        .offset:         16
        .size:           8
        .value_kind:     global_buffer
      - .actual_access:  read_only
        .address_space:  global
        .offset:         24
        .size:           8
        .value_kind:     global_buffer
      - .actual_access:  read_only
        .address_space:  global
        .offset:         32
        .size:           8
        .value_kind:     global_buffer
      - .actual_access:  read_only
        .address_space:  global
        .offset:         40
        .size:           8
        .value_kind:     global_buffer
      - .actual_access:  read_only
        .address_space:  global
        .offset:         48
        .size:           8
        .value_kind:     global_buffer
      - .actual_access:  read_only
        .address_space:  global
        .offset:         56
        .size:           8
        .value_kind:     global_buffer
      - .actual_access:  read_only
        .address_space:  global
        .offset:         64
        .size:           8
        .value_kind:     global_buffer
      - .offset:         72
        .size:           4
        .value_kind:     by_value
      - .offset:         76
        .size:           4
        .value_kind:     by_value
      - .offset:         80
        .size:           4
        .value_kind:     by_value
      - .offset:         88
        .size:           4
        .value_kind:     hidden_block_count_x
      - .offset:         92
        .size:           4
        .value_kind:     hidden_block_count_y
      - .offset:         96
        .size:           4
        .value_kind:     hidden_block_count_z
      - .offset:         100
        .size:           2
        .value_kind:     hidden_group_size_x
      - .offset:         102
        .size:           2
        .value_kind:     hidden_group_size_y
      - .offset:         104
        .size:           2
        .value_kind:     hidden_group_size_z
      - .offset:         106
        .size:           2
        .value_kind:     hidden_remainder_x
      - .offset:         108
        .size:           2
        .value_kind:     hidden_remainder_y
      - .offset:         110
        .size:           2
        .value_kind:     hidden_remainder_z
      - .offset:         128
        .size:           8
        .value_kind:     hidden_global_offset_x
      - .offset:         136
        .size:           8
        .value_kind:     hidden_global_offset_y
      - .offset:         144
        .size:           8
        .value_kind:     hidden_global_offset_z
      - .offset:         152
        .size:           2
        .value_kind:     hidden_grid_dims
      - .offset:         208
        .size:           4
        .value_kind:     hidden_dynamic_lds_size
    .group_segment_fixed_size: 0
    .kernarg_segment_align: 8
    .kernarg_segment_size: 344
    .language:       OpenCL C
    .language_version:
      - 2
      - 0
    .max_flat_workgroup_size: 512
    .name:           _Z12gemm_persistILi1ELi14336ELi32ELi16EEvPKDF16_S1_PvPKfS4_S4_S4_PDF16_S5_iii
    .private_segment_fixed_size: 0
    .sgpr_count:     68
    .sgpr_spill_count: 0
    .symbol:         _Z12gemm_persistILi1ELi14336ELi32ELi16EEvPKDF16_S1_PvPKfS4_S4_S4_PDF16_S5_iii.kd
    .uniform_work_group_size: 1
    .uses_dynamic_stack: false
    .vgpr_count:     236
    .vgpr_spill_count: 0
    .wavefront_size: 64
